# v_G plus g_job: eight w_in row loads per iteration issued together with counted waits
# baseline (speedup 1.0000x reference)
.LBB0_702:
	v_add_u32_e32 v34, s0, v46
	s_mov_b32 s1, 0x9000
	v_mad_i64_i32 v[42:43], s[64:65], v34, s1, v[48:49]
	global_load_dwordx4 v[60:63], v[42:43], off offset:16
	global_load_dwordx4 v[64:67], v[42:43], off
	global_load_dwordx4 v[68:71], v[42:43], off offset:144
	global_load_dwordx4 v[72:75], v[42:43], off offset:128
	global_load_dwordx4 v[76:79], v[42:43], off offset:272
	global_load_dwordx4 v[80:83], v[42:43], off offset:256
	global_load_dwordx4 v[84:87], v[42:43], off offset:400
	global_load_dwordx4 v[88:91], v[42:43], off offset:384
	s_add_i32 s0, s0, 16
	s_cmpk_lg_i32 s0, 0x80
	s_waitcnt vmcnt(6)
	v_bfe_u32 v44, v64, 16, 1
	v_add3_u32 v38, v64, v44, s6
	v_bfe_u32 v44, v65, 16, 1
	v_lshrrev_b32_e32 v38, 16, v38
	v_add3_u32 v39, v65, v44, s6
	v_and_or_b32 v38, v39, s7, v38
	v_bfe_u32 v39, v66, 16, 1
	v_add3_u32 v39, v66, v39, s6
	v_bfe_u32 v40, v67, 16, 1
	v_lshrrev_b32_e32 v39, 16, v39
	v_add3_u32 v40, v67, v40, s6
	v_and_or_b32 v39, v40, s7, v39
	v_bfe_u32 v40, v60, 16, 1
	v_add3_u32 v34, v60, v40, s6
	v_bfe_u32 v40, v61, 16, 1
	v_lshrrev_b32_e32 v34, 16, v34
	v_add3_u32 v35, v61, v40, s6
	v_and_or_b32 v40, v35, s7, v34
	v_bfe_u32 v34, v62, 16, 1
	v_add3_u32 v34, v62, v34, s6
	v_bfe_u32 v35, v63, 16, 1
	v_lshrrev_b32_e32 v34, 16, v34
	v_add3_u32 v35, v63, v35, s6
	v_and_or_b32 v41, v35, s7, v34
	s_nop 1
	v_mfma_f32_16x16x32_bf16 v[34:37], v[38:41], v[2:5], 0
	v_mfma_f32_16x16x32_bf16 v[34:37], v[38:41], v[6:9], v[34:37]
	s_waitcnt vmcnt(4)
	v_bfe_u32 v44, v72, 16, 1
	v_add3_u32 v44, v72, v44, s6
	v_bfe_u32 v45, v73, 16, 1
	v_lshrrev_b32_e32 v44, 16, v44
	v_add3_u32 v45, v73, v45, s6
	v_and_or_b32 v54, v45, s7, v44
	v_bfe_u32 v44, v74, 16, 1
	v_add3_u32 v44, v74, v44, s6
	v_bfe_u32 v45, v75, 16, 1
	v_lshrrev_b32_e32 v44, 16, v44
	v_add3_u32 v45, v75, v45, s6
	v_and_or_b32 v55, v45, s7, v44
	v_bfe_u32 v44, v68, 16, 1
	v_add3_u32 v38, v68, v44, s6
	v_bfe_u32 v44, v69, 16, 1
	v_lshrrev_b32_e32 v38, 16, v38
	v_add3_u32 v39, v69, v44, s6
	v_and_or_b32 v56, v39, s7, v38
	v_bfe_u32 v38, v70, 16, 1
	v_add3_u32 v38, v70, v38, s6
	v_bfe_u32 v39, v71, 16, 1
	v_lshrrev_b32_e32 v38, 16, v38
	v_add3_u32 v39, v71, v39, s6
	v_and_or_b32 v57, v39, s7, v38
	s_nop 1
	v_mfma_f32_16x16x32_bf16 v[34:37], v[54:57], v[10:13], v[34:37]
	v_mfma_f32_16x16x32_bf16 v[34:37], v[54:57], v[14:17], v[34:37]
	s_waitcnt vmcnt(2)
	v_bfe_u32 v44, v80, 16, 1
	v_add3_u32 v44, v80, v44, s6
	v_bfe_u32 v45, v81, 16, 1
	v_lshrrev_b32_e32 v44, 16, v44
	v_add3_u32 v45, v81, v45, s6
	v_and_or_b32 v54, v45, s7, v44
	v_bfe_u32 v44, v82, 16, 1
	v_add3_u32 v44, v82, v44, s6
	v_bfe_u32 v45, v83, 16, 1
	v_lshrrev_b32_e32 v44, 16, v44
	v_add3_u32 v45, v83, v45, s6
	v_and_or_b32 v55, v45, s7, v44
	v_bfe_u32 v44, v76, 16, 1
	v_add3_u32 v38, v76, v44, s6
	v_bfe_u32 v44, v77, 16, 1
	v_lshrrev_b32_e32 v38, 16, v38
	v_add3_u32 v39, v77, v44, s6
	v_and_or_b32 v56, v39, s7, v38
	v_bfe_u32 v38, v78, 16, 1
	v_add3_u32 v38, v78, v38, s6
	v_bfe_u32 v39, v79, 16, 1
	v_lshrrev_b32_e32 v38, 16, v38
	v_add3_u32 v39, v79, v39, s6
	v_and_or_b32 v57, v39, s7, v38
	s_nop 0
	v_mfma_f32_16x16x32_bf16 v[34:37], v[54:57], v[18:21], v[34:37]
	s_waitcnt vmcnt(0)
	v_bfe_u32 v53, v88, 16, 1
	v_add3_u32 v42, v88, v53, s6
	v_bfe_u32 v53, v89, 16, 1
	v_lshrrev_b32_e32 v42, 16, v42
	v_add3_u32 v43, v89, v53, s6
	v_and_or_b32 v42, v43, s7, v42
	v_bfe_u32 v43, v90, 16, 1
	v_add3_u32 v43, v90, v43, s6
	v_bfe_u32 v44, v91, 16, 1
	v_lshrrev_b32_e32 v43, 16, v43
	v_add3_u32 v44, v91, v44, s6
	v_and_or_b32 v43, v44, s7, v43
	v_bfe_u32 v44, v84, 16, 1
	v_add3_u32 v38, v84, v44, s6
	v_bfe_u32 v44, v85, 16, 1
	v_lshrrev_b32_e32 v38, 16, v38
	v_add3_u32 v39, v85, v44, s6
	v_and_or_b32 v44, v39, s7, v38
	v_bfe_u32 v38, v86, 16, 1
	v_add3_u32 v38, v86, v38, s6
	v_bfe_u32 v39, v87, 16, 1
	v_lshrrev_b32_e32 v38, 16, v38
	v_add3_u32 v39, v87, v39, s6
	v_and_or_b32 v45, v39, s7, v38
	v_mfma_f32_16x16x32_bf16 v[34:37], v[54:57], v[22:25], v[34:37]
	s_nop 0
	v_mfma_f32_16x16x32_bf16 v[34:37], v[42:45], v[26:29], v[34:37]
	v_mfma_f32_16x16x32_bf16 v[34:37], v[42:45], v[30:33], v[34:37]
	s_nop 7
	v_bfe_u32 v38, v34, 16, 1
	v_add3_u32 v34, v34, v38, s6
	v_bfe_u32 v38, v35, 16, 1
	v_lshrrev_b32_e32 v34, 16, v34
	v_add3_u32 v35, v35, v38, s6
	v_and_or_b32 v34, v35, s7, v34
	v_bfe_u32 v35, v36, 16, 1
	v_add3_u32 v35, v36, v35, s6
	v_bfe_u32 v36, v37, 16, 1
	v_lshrrev_b32_e32 v35, 16, v35
	v_add3_u32 v36, v37, v36, s6
	v_and_or_b32 v35, v36, s7, v35
	global_store_dwordx2 v[50:51], v[34:35], off
	v_lshl_add_u64 v[50:51], v[50:51], 0, 32
	s_cbranch_scc1 .LBB0_702
	s_add_i32 s60, s60, s33
	s_add_i32 s19, s19, s33
	s_cmpk_gt_i32 s60, 0xff
	s_cbranch_scc0 .LBB0_697
